# ssd_states tile-fill loops: all trips' loads issued up front and rotated through the consumer registers (on top of the DSA fast-path batches)
# speedup vs baseline: 1.0058x; 1.0058x over previous
.LBB0_1114:
	s_or_b64 exec, exec, s[10:11]
	v_or_b32_e32 v18, s6, v9
	s_waitcnt lgkmcnt(0)
	s_barrier
	s_and_saveexec_b64 s[10:11], vcc
	s_cbranch_execz .LBB0_1117
	v_mov_b64_e32 v[16:17], s[2:3]
	v_mad_i64_i32 v[16:17], s[4:5], v18, s24, v[16:17]
	s_lshl_b32 s6, s31, 8
	v_lshl_add_u64 v[16:17], v[16:17], 0, s[6:7]
	s_mov_b64 s[12:13], 0
	v_mov_b32_e32 v4, v1
	v_ashrrev_i32_e32 v11, 4, v4
	v_and_b32_e32 v20, -8, v11
	v_ashrrev_i32_e32 v21, 31, v20
	v_lshl_add_u64 v[248:249], v[20:21], 1, v[16:17]
	global_load_dwordx4 v[26:29], v[248:249], off offset:2048
	global_load_dwordx4 v[142:145], v[248:249], off offset:2112
	global_load_dwordx4 v[146:149], v[248:249], off offset:2176
	global_load_dwordx4 v[224:227], v[248:249], off offset:2240
.LBB0_1116:
	v_ashrrev_i32_e32 v11, 4, v4
	v_and_b32_e32 v20, -8, v11
	v_ashrrev_i32_e32 v21, 31, v20
	v_add_u32_e32 v11, 0x200, v4
	v_cmp_lt_i32_e64 s[4:5], s28, v4
	s_or_b64 s[12:13], s[4:5], s[12:13]
	v_mov_b32_e32 v4, v11
	v_mad_u64_u32 v[20:21], s[4:5], v20, s18, v[8:9]
	s_waitcnt vmcnt(0)
	ds_write_b16 v20, v26 offset:8192
	ds_write_b16_d16_hi v20, v26 offset:8464
	ds_write_b16 v20, v27 offset:8736
	ds_write_b16_d16_hi v20, v27 offset:9008
	ds_write_b16 v20, v28 offset:9280
	ds_write_b16_d16_hi v20, v28 offset:9552
	ds_write_b16 v20, v29 offset:9824
	ds_write_b16_d16_hi v20, v29 offset:10096
	v_mov_b64_e32 v[26:27], v[142:143]
	v_mov_b64_e32 v[28:29], v[144:145]
	v_mov_b64_e32 v[142:143], v[146:147]
	v_mov_b64_e32 v[144:145], v[148:149]
	v_mov_b64_e32 v[146:147], v[224:225]
	v_mov_b64_e32 v[148:149], v[226:227]
	s_andn2_b64 exec, exec, s[12:13]
	s_cbranch_execnz .LBB0_1116
.LBB0_1117:
	s_or_b64 exec, exec, s[10:11]
	s_lshl_b32 s4, s31, 10
	s_add_u32 s10, s2, s4
	s_addc_u32 s11, s3, 0
	s_waitcnt lgkmcnt(0)
	s_barrier
	s_and_saveexec_b64 s[12:13], s[0:1]
	s_cbranch_execz .LBB0_1120
	v_mov_b64_e32 v[16:17], s[10:11]
	v_mad_i64_i32 v[16:17], s[4:5], v18, s24, v[16:17]
	s_mov_b64 s[14:15], 0
	v_mov_b32_e32 v4, v1
	v_ashrrev_i32_e32 v11, 4, v4
	v_and_b32_e32 v20, -8, v11
	v_ashrrev_i32_e32 v21, 31, v20
	v_lshl_add_u64 v[248:249], v[20:21], 1, v[16:17]
	global_load_dwordx4 v[26:29], v[248:249], off
	global_load_dwordx4 v[142:145], v[248:249], off offset:64
	global_load_dwordx4 v[146:149], v[248:249], off offset:128
	global_load_dwordx4 v[224:227], v[248:249], off offset:192
	global_load_dwordx4 v[228:231], v[248:249], off offset:256
	global_load_dwordx4 v[232:235], v[248:249], off offset:320
	global_load_dwordx4 v[236:239], v[248:249], off offset:384
	global_load_dwordx4 v[240:243], v[248:249], off offset:448
.LBB0_1119:
	v_ashrrev_i32_e32 v11, 4, v4
	v_and_b32_e32 v20, -8, v11
	v_ashrrev_i32_e32 v21, 31, v20
	v_ashrrev_i32_e32 v13, 10, v4
	v_add_u32_e32 v15, 0x200, v4
	v_add_u32_e32 v19, v13, v22
	v_cmp_lt_i32_e64 s[4:5], s29, v4
	v_lshl_add_u32 v13, v13, 2, 0
	v_mov_b32_e32 v4, v15
	v_lshl_add_u32 v15, v19, 2, 0
	ds_read_b32 v13, v13 offset:4064
	ds_read2st64_b32 v[32:33], v15 offset1:16
	v_or_b32_e32 v11, 7, v11
	s_or_b64 s[14:15], s[4:5], s[14:15]
	v_mad_u64_u32 v[30:31], s[4:5], v11, s18, v[8:9]
	s_waitcnt lgkmcnt(0)
	v_sub_f32_e32 v11, v13, v32
	v_mul_f32_e32 v13, 0x3fb8aa3b, v11
	v_fma_f32 v15, v11, s25, -v13
	v_rndne_f32_e32 v19, v13
	v_fmac_f32_e32 v15, 0x32a5705f, v11
	v_sub_f32_e32 v13, v13, v19
	v_add_f32_e32 v13, v13, v15
	v_cvt_i32_f32_e32 v19, v19
	v_exp_f32_e32 v13, v13
	v_mad_u64_u32 v[20:21], s[4:5], v20, s18, v[8:9]
	v_cmp_ngt_f32_e64 s[4:5], s26, v11
	v_ldexp_f32 v13, v13, v19
	s_waitcnt vmcnt(0)
	v_and_b32_e32 v15, 0xffff0000, v26
	v_cndmask_b32_e64 v13, 0, v13, s[4:5]
	v_cmp_nlt_f32_e64 s[4:5], s27, v11
	v_lshlrev_b32_e32 v19, 16, v27
	v_and_b32_e32 v21, 0xffff0000, v27
	v_cndmask_b32_e64 v11, v23, v13, s[4:5]
	v_mul_f32_e32 v11, v33, v11
	v_lshlrev_b32_e32 v13, 16, v26
	v_lshlrev_b32_e32 v26, 16, v28
	v_and_b32_e32 v27, 0xffff0000, v28
	v_lshlrev_b32_e32 v28, 16, v29
	v_and_b32_e32 v29, 0xffff0000, v29
	v_mul_f32_e32 v13, v11, v13
	v_mul_f32_e32 v15, v11, v15
	v_mul_f32_e32 v19, v11, v19
	v_mul_f32_e32 v21, v11, v21
	v_mul_f32_e32 v26, v11, v26
	v_mul_f32_e32 v27, v11, v27
	v_mul_f32_e32 v28, v11, v28
	v_mul_f32_e32 v11, v11, v29
	v_cvt_pk_bf16_f32 v13, v13, s0
	v_cvt_pk_bf16_f32 v15, v15, s0
	v_cvt_pk_bf16_f32 v19, v19, s0
	v_cvt_pk_bf16_f32 v21, v21, s0
	v_cvt_pk_bf16_f32 v26, v26, s0
	v_cvt_pk_bf16_f32 v27, v27, s0
	v_cvt_pk_bf16_f32 v28, v28, s0
	v_cvt_pk_bf16_f32 v11, v11, s0
	ds_write_b16 v20, v13 offset:43008
	ds_write_b16 v20, v15 offset:43280
	ds_write_b16 v20, v19 offset:43552
	ds_write_b16 v20, v21 offset:43824
	ds_write_b16 v20, v26 offset:44096
	ds_write_b16 v20, v27 offset:44368
	ds_write_b16 v20, v28 offset:44640
	ds_write_b16 v30, v11 offset:43008
	v_mov_b64_e32 v[26:27], v[142:143]
	v_mov_b64_e32 v[28:29], v[144:145]
	v_mov_b64_e32 v[142:143], v[146:147]
	v_mov_b64_e32 v[144:145], v[148:149]
	v_mov_b64_e32 v[146:147], v[224:225]
	v_mov_b64_e32 v[148:149], v[226:227]
	v_mov_b64_e32 v[224:225], v[228:229]
	v_mov_b64_e32 v[226:227], v[230:231]
	v_mov_b64_e32 v[228:229], v[232:233]
	v_mov_b64_e32 v[230:231], v[234:235]
	v_mov_b64_e32 v[232:233], v[236:237]
	v_mov_b64_e32 v[234:235], v[238:239]
	v_mov_b64_e32 v[236:237], v[240:241]
	v_mov_b64_e32 v[238:239], v[242:243]
	s_andn2_b64 exec, exec, s[14:15]
	s_cbranch_execnz .LBB0_1119
.LBB0_1120:
	s_or_b64 exec, exec, s[12:13]
	s_waitcnt lgkmcnt(0)
	s_barrier
	ds_read_b128 v[26:29], v25 offset:8192
	ds_read_b128 v[30:33], v24 offset:43008
	ds_read_b128 v[34:37], v24 offset:43072
	ds_read_b128 v[38:41], v25 offset:8256
	ds_read_b128 v[46:49], v25 offset:12544
	ds_read_b128 v[50:53], v25 offset:12608
	ds_read_b128 v[58:61], v25 offset:16896
	ds_read_b128 v[62:65], v25 offset:16960
	ds_read_b128 v[70:73], v25 offset:21248
	ds_read_b128 v[74:77], v25 offset:21312
	ds_read_b128 v[78:81], v24 offset:47360
	ds_read_b128 v[82:85], v24 offset:47424
	ds_read_b128 v[98:101], v24 offset:51712
	ds_read_b128 v[102:105], v24 offset:51776
	ds_read_b128 v[118:121], v24 offset:56064
	ds_read_b128 v[122:125], v24 offset:56128
	s_waitcnt lgkmcnt(14)
	v_mfma_f32_16x16x32_bf16 v[42:45], v[26:29], v[30:33], 0
	s_lshl_b32 s4, s31, 3
	s_lshl_b32 s5, s8, 4
	s_or_b32 s4, s5, s4
	s_waitcnt lgkmcnt(11)
	v_mfma_f32_16x16x32_bf16 v[54:57], v[46:49], v[30:33], 0
	v_add_u32_e32 v16, s4, v3
	v_ashrrev_i32_e32 v17, 31, v16
	v_lshlrev_b64 v[20:21], 15, v[16:17]
	s_waitcnt lgkmcnt(9)
	v_mfma_f32_16x16x32_bf16 v[66:69], v[58:61], v[30:33], 0
	v_lshl_add_u64 v[20:21], v[6:7], 0, v[20:21]
	v_lshlrev_b32_e32 v4, 2, v2
	v_mov_b32_e32 v11, v5
	s_waitcnt lgkmcnt(7)
	v_mfma_f32_16x16x32_bf16 v[30:33], v[70:73], v[30:33], 0
	v_mov_b32_e32 v13, v5
	v_mov_b32_e32 v15, v5
	s_waitcnt lgkmcnt(5)
	v_mfma_f32_16x16x32_bf16 v[86:89], v[26:29], v[78:81], 0
	v_mfma_f32_16x16x32_bf16 v[90:93], v[46:49], v[78:81], 0
	v_mfma_f32_16x16x32_bf16 v[94:97], v[58:61], v[78:81], 0
	v_mfma_f32_16x16x32_bf16 v[78:81], v[70:73], v[78:81], 0
	s_waitcnt lgkmcnt(3)
	v_mfma_f32_16x16x32_bf16 v[106:109], v[26:29], v[98:101], 0
	v_mfma_f32_16x16x32_bf16 v[110:113], v[46:49], v[98:101], 0
	s_waitcnt lgkmcnt(1)
	v_mfma_f32_16x16x32_bf16 v[26:29], v[26:29], v[118:121], 0
	v_mfma_f32_16x16x32_bf16 v[46:49], v[46:49], v[118:121], 0
	v_mfma_f32_16x16x32_bf16 v[42:45], v[38:41], v[34:37], v[42:45]
	v_mfma_f32_16x16x32_bf16 v[54:57], v[50:53], v[34:37], v[54:57]
	v_mfma_f32_16x16x32_bf16 v[66:69], v[62:65], v[34:37], v[66:69]
	v_mfma_f32_16x16x32_bf16 v[30:33], v[74:77], v[34:37], v[30:33]
	v_mfma_f32_16x16x32_bf16 v[34:37], v[38:41], v[82:85], v[86:89]
	v_mfma_f32_16x16x32_bf16 v[86:89], v[50:53], v[82:85], v[90:93]
	v_mfma_f32_16x16x32_bf16 v[90:93], v[62:65], v[82:85], v[94:97]
	v_mfma_f32_16x16x32_bf16 v[78:81], v[74:77], v[82:85], v[78:81]
	v_mfma_f32_16x16x32_bf16 v[82:85], v[38:41], v[102:105], v[106:109]
	v_mfma_f32_16x16x32_bf16 v[94:97], v[50:53], v[102:105], v[110:113]
	s_waitcnt lgkmcnt(0)
	v_mfma_f32_16x16x32_bf16 v[26:29], v[38:41], v[122:125], v[26:29]
	v_mfma_f32_16x16x32_bf16 v[38:41], v[50:53], v[122:125], v[46:49]
	ds_read_b128 v[50:53], v25 offset:8320
	v_mfma_f32_16x16x32_bf16 v[114:117], v[58:61], v[98:101], 0
	v_mfma_f32_16x16x32_bf16 v[98:101], v[70:73], v[98:101], 0
	v_mfma_f32_16x16x32_bf16 v[58:61], v[58:61], v[118:121], 0
	v_mfma_f32_16x16x32_bf16 v[70:73], v[70:73], v[118:121], 0
	v_mfma_f32_16x16x32_bf16 v[106:109], v[62:65], v[102:105], v[114:117]
	v_mfma_f32_16x16x32_bf16 v[98:101], v[74:77], v[102:105], v[98:101]
	v_mfma_f32_16x16x32_bf16 v[46:49], v[62:65], v[122:125], v[58:61]
	v_mfma_f32_16x16x32_bf16 v[58:61], v[74:77], v[122:125], v[70:73]
	ds_read_b128 v[62:65], v24 offset:43136
	s_nop 2
	ds_read_b128 v[70:73], v24 offset:43200
	ds_read_b128 v[74:77], v25 offset:8384
	ds_read_b128 v[102:105], v25 offset:12672
	ds_read_b128 v[110:113], v25 offset:12736
	ds_read_b128 v[114:117], v25 offset:17024
	ds_read_b128 v[118:121], v25 offset:17088
	ds_read_b128 v[122:125], v25 offset:21376
	ds_read_b128 v[126:129], v25 offset:21440
	s_waitcnt lgkmcnt(8)
	v_mfma_f32_16x16x32_bf16 v[42:45], v[50:53], v[62:65], v[42:45]
	s_waitcnt lgkmcnt(5)
	v_mfma_f32_16x16x32_bf16 v[54:57], v[102:105], v[62:65], v[54:57]
	s_waitcnt lgkmcnt(3)
	v_mfma_f32_16x16x32_bf16 v[66:69], v[114:117], v[62:65], v[66:69]
	s_waitcnt lgkmcnt(1)
	v_mfma_f32_16x16x32_bf16 v[30:33], v[122:125], v[62:65], v[30:33]
	ds_read_b128 v[62:65], v24 offset:47488
	ds_read_b128 v[130:133], v24 offset:47552
	s_waitcnt lgkmcnt(1)
	v_mfma_f32_16x16x32_bf16 v[34:37], v[50:53], v[62:65], v[34:37]
	v_mfma_f32_16x16x32_bf16 v[86:89], v[102:105], v[62:65], v[86:89]
	v_mfma_f32_16x16x32_bf16 v[90:93], v[114:117], v[62:65], v[90:93]
	v_mfma_f32_16x16x32_bf16 v[62:65], v[122:125], v[62:65], v[78:81]
	s_nop 2
	ds_read_b128 v[78:81], v24 offset:51840
	ds_read_b128 v[134:137], v24 offset:51904
	s_waitcnt lgkmcnt(1)
	v_mfma_f32_16x16x32_bf16 v[82:85], v[50:53], v[78:81], v[82:85]
	v_mfma_f32_16x16x32_bf16 v[94:97], v[102:105], v[78:81], v[94:97]
	v_mfma_f32_16x16x32_bf16 v[106:109], v[114:117], v[78:81], v[106:109]
	v_mfma_f32_16x16x32_bf16 v[78:81], v[122:125], v[78:81], v[98:101]
	s_nop 2
	ds_read_b128 v[98:101], v24 offset:56192
	ds_read_b128 v[138:141], v24 offset:56256
	v_mfma_f32_16x16x32_bf16 v[42:45], v[74:77], v[70:73], v[42:45]
	v_mfma_f32_16x16x32_bf16 v[54:57], v[110:113], v[70:73], v[54:57]
	v_mfma_f32_16x16x32_bf16 v[30:33], v[126:129], v[70:73], v[30:33]
	v_mfma_f32_16x16x32_bf16 v[34:37], v[74:77], v[130:133], v[34:37]
	s_waitcnt lgkmcnt(1)
	v_mfma_f32_16x16x32_bf16 v[26:29], v[50:53], v[98:101], v[26:29]
	v_mfma_f32_16x16x32_bf16 v[50:53], v[122:125], v[98:101], v[58:61]
	v_mfma_f32_16x16x32_bf16 v[58:61], v[118:121], v[70:73], v[66:69]
	v_mfma_f32_16x16x32_bf16 v[66:69], v[110:113], v[130:133], v[86:89]
	v_mfma_f32_16x16x32_bf16 v[70:73], v[118:121], v[130:133], v[90:93]
	s_nop 1
	v_lshl_add_u64 v[86:87], v[20:21], 0, v[4:5]
	global_store_dwordx4 v[86:87], v[42:45], off
	global_store_dwordx4 v[86:87], v[54:57], off offset:64
	s_nop 0
	global_store_dwordx4 v[86:87], v[58:61], off offset:128
	global_store_dwordx4 v[86:87], v[30:33], off offset:192
	v_mfma_f32_16x16x32_bf16 v[62:65], v[126:129], v[130:133], v[62:65]
	v_lshl_add_u64 v[54:55], v[20:21], 0, v[10:11]
	global_store_dwordx4 v[54:55], v[34:37], off
	global_store_dwordx4 v[54:55], v[66:69], off offset:64
	global_store_dwordx4 v[54:55], v[70:73], off offset:128
	v_mfma_f32_16x16x32_bf16 v[38:41], v[102:105], v[98:101], v[38:41]
	s_nop 2
	global_store_dwordx4 v[54:55], v[62:65], off offset:192
	v_lshl_add_u64 v[54:55], v[20:21], 0, v[12:13]
	v_lshl_add_u64 v[20:21], v[20:21], 0, v[14:15]
	v_mfma_f32_16x16x32_bf16 v[82:85], v[74:77], v[134:137], v[82:85]
	v_mfma_f32_16x16x32_bf16 v[46:49], v[114:117], v[98:101], v[46:49]
	v_mfma_f32_16x16x32_bf16 v[42:45], v[110:113], v[134:137], v[94:97]
	v_mfma_f32_16x16x32_bf16 v[34:37], v[126:129], v[134:137], v[78:81]
	v_mfma_f32_16x16x32_bf16 v[30:33], v[118:121], v[134:137], v[106:109]
	s_nop 3
	global_store_dwordx4 v[54:55], v[82:85], off
	s_nop 0
	global_store_dwordx4 v[54:55], v[42:45], off offset:64
	s_nop 0
	global_store_dwordx4 v[54:55], v[30:33], off offset:128
	global_store_dwordx4 v[54:55], v[34:37], off offset:192
	s_waitcnt lgkmcnt(0)
	v_mfma_f32_16x16x32_bf16 v[26:29], v[74:77], v[138:141], v[26:29]
	v_mfma_f32_16x16x32_bf16 v[30:33], v[110:113], v[138:141], v[38:41]
	v_mfma_f32_16x16x32_bf16 v[34:37], v[118:121], v[138:141], v[46:49]
	s_nop 5
	global_store_dwordx4 v[20:21], v[26:29], off
	global_store_dwordx4 v[20:21], v[30:33], off offset:64
	global_store_dwordx4 v[20:21], v[34:37], off offset:128
	v_mfma_f32_16x16x32_bf16 v[26:29], v[126:129], v[138:141], v[50:53]
	s_nop 7
	global_store_dwordx4 v[20:21], v[26:29], off offset:192
	s_barrier
	s_and_saveexec_b64 s[8:9], s[0:1]
	s_cbranch_execz .LBB0_1096
	v_mov_b64_e32 v[20:21], s[10:11]
	v_mad_i64_i32 v[18:19], s[4:5], v18, s24, v[20:21]
	s_mov_b64 s[10:11], 0
	v_mov_b32_e32 v11, v1
	v_ashrrev_i32_e32 v13, 4, v11
	v_and_b32_e32 v20, -8, v13
	v_ashrrev_i32_e32 v21, 31, v20
	v_lshl_add_u64 v[248:249], v[20:21], 1, v[18:19]
	global_load_dwordx4 v[26:29], v[248:249], off offset:512
	global_load_dwordx4 v[142:145], v[248:249], off offset:576
	global_load_dwordx4 v[146:149], v[248:249], off offset:640
	global_load_dwordx4 v[224:227], v[248:249], off offset:704
	global_load_dwordx4 v[228:231], v[248:249], off offset:768
	global_load_dwordx4 v[232:235], v[248:249], off offset:832
	global_load_dwordx4 v[236:239], v[248:249], off offset:896
	global_load_dwordx4 v[240:243], v[248:249], off offset:960
.LBB0_1122:
	v_ashrrev_i32_e32 v13, 4, v11
	v_and_b32_e32 v20, -8, v13
	v_ashrrev_i32_e32 v21, 31, v20
	v_ashrrev_i32_e32 v15, 10, v11
	v_add_u32_e32 v17, 0x200, v11
	v_add_u32_e32 v21, v15, v22
	v_cmp_lt_i32_e64 s[4:5], s29, v11
	v_or_b32_e32 v13, 7, v13
	v_mov_b32_e32 v11, v17
	v_lshl_add_u32 v17, v21, 2, 0
	v_lshl_add_u32 v15, v15, 2, 0
	s_or_b64 s[10:11], s[4:5], s[10:11]
	v_mad_u64_u32 v[30:31], s[4:5], v13, s18, v[8:9]
	v_add_u32_e32 v13, 16, v17
	ds_read_b32 v15, v15 offset:4080
	ds_read2st64_b32 v[32:33], v13 offset1:16
	v_mad_u64_u32 v[20:21], s[4:5], v20, s18, v[8:9]
	s_waitcnt lgkmcnt(0)
	v_sub_f32_e32 v13, v15, v32
	v_mul_f32_e32 v15, 0x3fb8aa3b, v13
	v_fma_f32 v17, v13, s25, -v15
	v_rndne_f32_e32 v21, v15
	v_fmac_f32_e32 v17, 0x32a5705f, v13
	v_sub_f32_e32 v15, v15, v21
	v_add_f32_e32 v15, v15, v17
	v_cvt_i32_f32_e32 v21, v21
	v_exp_f32_e32 v15, v15
	v_cmp_ngt_f32_e64 s[4:5], s26, v13
	v_ldexp_f32 v15, v15, v21
	s_nop 0
	v_cndmask_b32_e64 v15, 0, v15, s[4:5]
	v_cmp_nlt_f32_e64 s[4:5], s27, v13
	s_waitcnt vmcnt(0)
	v_and_b32_e32 v17, 0xffff0000, v26
	v_cndmask_b32_e64 v13, v23, v15, s[4:5]
	v_mul_f32_e32 v13, v33, v13
	v_lshlrev_b32_e32 v15, 16, v26
	v_lshlrev_b32_e32 v21, 16, v27
	v_and_b32_e32 v26, 0xffff0000, v27
	v_lshlrev_b32_e32 v27, 16, v28
	v_and_b32_e32 v28, 0xffff0000, v28
	v_lshlrev_b32_e32 v31, 16, v29
	v_and_b32_e32 v29, 0xffff0000, v29
	v_mul_f32_e32 v15, v13, v15
	v_mul_f32_e32 v17, v13, v17
	v_mul_f32_e32 v21, v13, v21
	v_mul_f32_e32 v26, v13, v26
	v_mul_f32_e32 v27, v13, v27
	v_mul_f32_e32 v28, v13, v28
	v_mul_f32_e32 v31, v13, v31
	v_mul_f32_e32 v13, v13, v29
	v_cvt_pk_bf16_f32 v15, v15, s0
	v_cvt_pk_bf16_f32 v17, v17, s0
	v_cvt_pk_bf16_f32 v21, v21, s0
	v_cvt_pk_bf16_f32 v26, v26, s0
	v_cvt_pk_bf16_f32 v27, v27, s0
	v_cvt_pk_bf16_f32 v28, v28, s0
	v_cvt_pk_bf16_f32 v29, v31, s0
	v_cvt_pk_bf16_f32 v13, v13, s0
	ds_write_b16 v20, v15 offset:43008
	ds_write_b16 v20, v17 offset:43280
	ds_write_b16 v20, v21 offset:43552
	ds_write_b16 v20, v26 offset:43824
	ds_write_b16 v20, v27 offset:44096
	ds_write_b16 v20, v28 offset:44368
	ds_write_b16 v20, v29 offset:44640
	ds_write_b16 v30, v13 offset:43008
	v_mov_b64_e32 v[26:27], v[142:143]
	v_mov_b64_e32 v[28:29], v[144:145]
	v_mov_b64_e32 v[142:143], v[146:147]
	v_mov_b64_e32 v[144:145], v[148:149]
	v_mov_b64_e32 v[146:147], v[224:225]
	v_mov_b64_e32 v[148:149], v[226:227]
	v_mov_b64_e32 v[224:225], v[228:229]
	v_mov_b64_e32 v[226:227], v[230:231]
	v_mov_b64_e32 v[228:229], v[232:233]
	v_mov_b64_e32 v[230:231], v[234:235]
	v_mov_b64_e32 v[232:233], v[236:237]
	v_mov_b64_e32 v[234:235], v[238:239]
	v_mov_b64_e32 v[236:237], v[240:241]
	v_mov_b64_e32 v[238:239], v[242:243]
	s_andn2_b64 exec, exec, s[10:11]
	s_cbranch_execnz .LBB0_1122
	s_branch .LBB0_1096
